# attention K-read LDS bank-conflict swizzle + MoE unit scheduler via ballot
# speedup vs baseline: 1.0073x; 1.0073x over previous
.LBB0_411:
	s_or_b64 exec, exec, s[56:57]
	v_readlane_b32 s23, v254, 12
	s_mov_b32 s70, s59
	s_waitcnt lgkmcnt(0)
	s_barrier
	v_mbcnt_lo_u32_b32 v49, -1, 0
	v_mbcnt_hi_u32_b32 v49, -1, v49
	s_lshr_b32 s6, s70, 5
	s_and_b32 s7, s70, 31
	s_mulk_i32 s6, 0xc00
	s_or_b32 s24, s6, s7
	s_mul_hi_i32 s6, s24, 0x2aaaaaab
	s_lshr_b32 s8, s6, 31
	s_ashr_i32 s6, s6, 5
	s_add_i32 s8, s6, s8
	s_mul_i32 s6, s8, 0xffffff40
	s_add_i32 s6, s6, s24
	s_ashr_i32 s30, s6, 6
	s_ashr_i32 s10, s8, 4
	s_cmp_eq_u32 s30, 1
	s_cselect_b32 s9, 3, 15
	s_cselect_b32 s11, 2, 4
	s_cmp_lt_u32 s6, 64
	s_cselect_b32 s12, 0, s11
	s_cselect_b32 s6, 0, s9
	s_lshr_b32 s25, s7, s12
	v_lshl_add_u32 v50, s23, 6, v49
	v_sub_u32_e64 v0, s25, 1 clamp
	s_ashr_i32 s9, s8, 31
	v_lshlrev_b32_e32 v4, 7, v0
	v_bfe_u32 v172, v50, 3, 7
	s_and_b32 s13, s6, s70
	s_lshl_b64 s[6:7], s[8:9], 13
	v_or_b32_e32 v0, v4, v172
	s_or_b32 s6, s6, s13
	v_lshlrev_b32_e32 v51, 3, v49
	v_lshlrev_b32_e32 v64, s12, v0
	v_and_b32_e32 v48, 56, v51
	v_lshl_add_u64 v[0:1], s[6:7], 0, v[64:65]
	v_lshlrev_b64 v[0:1], 7, v[0:1]
	v_lshlrev_b32_e32 v5, 1, v48
	v_or_b32_e32 v0, v0, v5
	v_add_u32_e32 v52, 0x200, v50
	v_lshl_add_u64 v[2:3], s[76:77], 0, v[0:1]
	v_lshl_add_u64 v[0:1], s[78:79], 0, v[0:1]
	v_bfe_u32 v174, v52, 3, 7
	s_barrier
	global_load_dwordx4 v[16:19], v[2:3], off
	global_load_dwordx4 v[20:23], v[0:1], off
	v_or_b32_e32 v0, v4, v174
	v_lshlrev_b32_e32 v64, s12, v0
	v_lshl_add_u64 v[0:1], s[6:7], 0, v[64:65]
	v_lshlrev_b64 v[0:1], 7, v[0:1]
	v_or_b32_e32 v0, v0, v5
	v_lshl_add_u64 v[2:3], s[76:77], 0, v[0:1]
	v_lshl_add_u64 v[0:1], s[78:79], 0, v[0:1]
	s_lshl_b32 s14, s25, 7
	global_load_dwordx4 v[24:27], v[2:3], off
	global_load_dwordx4 v[28:31], v[0:1], off
	v_or_b32_e32 v0, s14, v172
	v_lshlrev_b32_e32 v64, s12, v0
	v_lshl_add_u64 v[0:1], s[6:7], 0, v[64:65]
	v_lshlrev_b64 v[0:1], 7, v[0:1]
	v_or_b32_e32 v0, v0, v5
	v_add_u32_e32 v53, 0x600, v50
	v_lshl_add_u64 v[2:3], s[76:77], 0, v[0:1]
	v_lshl_add_u64 v[0:1], s[78:79], 0, v[0:1]
	v_bfe_u32 v175, v53, 3, 7
	global_load_dwordx4 v[32:35], v[2:3], off
	global_load_dwordx4 v[36:39], v[0:1], off
	v_or_b32_e32 v0, s14, v175
	v_lshlrev_b32_e32 v64, s12, v0
	v_lshl_add_u64 v[0:1], s[6:7], 0, v[64:65]
	v_lshlrev_b64 v[0:1], 7, v[0:1]
	v_or_b32_e32 v0, v0, v5
	v_bfe_u32 v56, v49, 4, 2
	v_lshl_add_u64 v[2:3], s[76:77], 0, v[0:1]
	v_lshl_add_u64 v[0:1], s[78:79], 0, v[0:1]
	v_and_b32_e32 v55, 15, v49
	v_lshlrev_b32_e32 v57, 2, v56
	global_load_dwordx4 v[40:43], v[2:3], off
	global_load_dwordx4 v[44:47], v[0:1], off
	v_cmp_lt_u32_e32 vcc, v57, v55
	v_mov_b32_e32 v8, 0xfe967699
	v_cmp_gt_u32_e64 s[6:7], v57, v55
	v_or_b32_e32 v1, 1, v57
	v_or_b32_e32 v2, 2, v57
	v_cndmask_b32_e32 v4, 0, v8, vcc
	v_cndmask_b32_e64 v0, 0, v8, s[6:7]
	v_cmp_lt_u32_e64 s[6:7], v1, v55
	v_cndmask_b32_e64 v1, v8, 0, vcc
	v_cmp_lt_u32_e32 vcc, v2, v55
	v_or_b32_e32 v3, 3, v57
	s_ashr_i32 s11, s10, 31
	v_cndmask_b32_e32 v6, 0, v8, vcc
	v_cmp_gt_u32_e32 vcc, v2, v55
	v_cndmask_b32_e64 v5, 0, v8, s[6:7]
	s_lshl_b64 s[6:7], s[10:11], 13
	v_cndmask_b32_e32 v2, 0, v8, vcc
	v_cmp_lt_u32_e32 vcc, v3, v55
	s_lshl_b32 s10, s23, 4
	s_add_i32 s14, s14, s10
	v_cndmask_b32_e32 v7, 0, v8, vcc
	v_cmp_gt_u32_e32 vcc, v3, v55
	s_or_b32 s6, s6, s13
	v_and_b32_e32 v160, 48, v49
	v_lshrrev_b32_e32 v204, 2, v55
	v_lshrrev_b32_e32 v205, 3, v55
	v_xor_b32_e32 v204, v204, v205
	v_and_b32_e32 v204, 1, v204
	v_lshlrev_b32_e32 v204, 4, v204
	v_xor_b32_e32 v215, v160, v204
	v_cndmask_b32_e32 v3, 0, v8, vcc
	v_or_b32_e32 v8, s14, v55
	v_ashrrev_i32_e32 v9, 31, v8
	v_lshlrev_b64 v[8:9], s12, v[8:9]
	v_lshl_add_u64 v[166:167], s[6:7], 0, v[8:9]
	s_lshl_b64 s[6:7], s[8:9], 20
	s_add_u32 s6, s64, s6
	v_lshlrev_b32_e32 v8, 7, v166
	s_addc_u32 s7, s65, s7
	v_and_b32_e32 v64, 0xfff80, v8
	v_lshl_add_u64 v[8:9], s[6:7], 0, v[64:65]
	v_mov_b32_e32 v161, v65
	v_lshl_add_u64 v[12:13], v[8:9], 0, v[160:161]
	global_load_dwordx4 v[8:11], v[12:13], off
	s_nop 0
	global_load_dwordx4 v[12:15], v[12:13], off offset:64
	v_lshrrev_b32_e32 v58, 3, v50
	v_add_u32_e32 v59, 0x400, v50
	v_lshlrev_b32_e32 v50, 3, v56
	v_lshlrev_b32_e32 v56, 4, v49
	s_movk_i32 s26, 0x90
	v_lshrrev_b32_e32 v52, 3, v52
	v_and_b32_e32 v176, 0x70, v56
	v_lshrrev_b32_e32 v204, 2, v58
	v_lshrrev_b32_e32 v205, 3, v58
	v_xor_b32_e32 v204, v204, v205
	v_and_b32_e32 v204, 1, v204
	v_lshlrev_b32_e32 v204, 4, v204
	v_xor_b32_e32 v176, v176, v204
	v_mul_lo_u32 v177, v58, s26
	v_add3_u32 v56, 0, v177, v176
	v_mul_lo_u32 v178, v52, s26
	s_waitcnt vmcnt(0)
	ds_write_b128 v56, v[16:19]
	ds_write_b128 v56, v[20:23] offset:36864
	v_add3_u32 v16, 0, v178, v176
	s_add_i32 s6, s10, 16
	ds_write_b128 v16, v[24:27]
	ds_write_b128 v16, v[28:31] offset:36864
	v_lshrrev_b32_e32 v16, 3, v59
	v_or_b32_e32 v17, s6, v55
	s_add_i32 s6, s10, 32
	v_lshrrev_b32_e32 v53, 3, v53
	v_mul_lo_u32 v179, v16, s26
	v_mul_lo_u32 v183, v17, s26
	v_or_b32_e32 v17, s6, v55
	s_add_i32 s6, s10, 48
	v_add3_u32 v16, 0, v179, v176
	v_mul_lo_u32 v180, v53, s26
	v_mul_lo_u32 v184, v17, s26
	v_or_b32_e32 v17, s6, v55
	s_add_i32 s6, s10, 64
	ds_write_b128 v16, v[32:35]
	ds_write_b128 v16, v[36:39] offset:36864
	v_add3_u32 v16, 0, v180, v176
	v_mul_lo_u32 v185, v17, s26
	v_or_b32_e32 v17, s6, v55
	s_add_i32 s6, s10, 0x50
	ds_write_b128 v16, v[40:43]
	ds_write_b128 v16, v[44:47] offset:36864
	v_bfe_u32 v16, v49, 2, 2
	v_mul_lo_u32 v186, v17, s26
	v_or_b32_e32 v17, s6, v55
	s_add_i32 s6, s10, 0x60
	s_and_b32 s22, s8, 15
	v_or_b32_e32 v181, s10, v55
	v_or3_b32 v16, v16, s10, v57
	v_mul_lo_u32 v187, v17, s26
	v_or_b32_e32 v17, s6, v55
	s_add_i32 s6, s10, 0x70
	s_addk_i32 s10, 0x80
	s_cmp_lt_i32 s23, 8
	s_cselect_b64 s[20:21], -1, 0
	s_cmp_lt_i32 s23, 7
	s_cselect_b64 s[18:19], -1, 0
	s_cmp_lt_i32 s23, 6
	s_cselect_b64 s[16:17], -1, 0
	s_cmp_lt_i32 s23, 5
	s_cselect_b64 s[14:15], -1, 0
	s_cmp_lt_i32 s23, 4
	v_mul_lo_u32 v188, v17, s26
	v_or_b32_e32 v17, s6, v55
	s_cselect_b64 s[12:13], -1, 0
	s_cmp_lt_i32 s23, 3
	v_mul_lo_u32 v189, v17, s26
	v_or_b32_e32 v17, s10, v55
	s_cselect_b64 s[10:11], -1, 0
	s_cmp_lt_i32 s23, 2
	v_and_b32_e32 v54, 63, v49
	s_cselect_b64 s[8:9], -1, 0
	s_cmp_lt_i32 s23, 1
	s_mov_b32 s71, s63
	s_mov_b32 s38, 0
	v_and_b32_e32 v171, 24, v51
	v_lshrrev_b32_e32 v204, 4, v49
	v_lshrrev_b32_e32 v205, 5, v49
	v_xor_b32_e32 v204, v204, v205
	v_and_b32_e32 v204, 1, v204
	v_lshlrev_b32_e32 v204, 4, v204
	v_xor_b32_e32 v171, v171, v204
	v_cmp_gt_u32_e32 vcc, 16, v54
	v_mul_lo_u32 v182, v181, s26
	v_mul_lo_u32 v190, v17, s26
	s_cselect_b64 s[6:7], -1, 0
	v_mul_lo_u32 v173, v16, s26
	s_or_b32 s39, s24, 32
	v_lshlrev_b32_e32 v191, 1, v48
	v_lshlrev_b32_e32 v168, 1, v50
	s_waitcnt lgkmcnt(0)
	s_barrier
.LBB0_412:
	s_mul_hi_i32 s23, s39, 0x2aaaaaab
	s_lshr_b32 s24, s23, 31
	s_ashr_i32 s23, s23, 5
	s_add_i32 s34, s23, s24
	s_mul_i32 s23, s34, 0xffffff40
	s_add_i32 s23, s39, s23
	s_mov_b32 s31, s25
	s_and_b32 s49, s38, 1
	s_ashr_i32 s24, s23, 6
	s_and_b32 s25, s39, 63
	s_ashr_i32 s36, s34, 4
	s_cmp_eq_u32 s24, 1
	s_cselect_b64 s[26:27], -1, 0
	s_and_b64 s[28:29], s[26:27], exec
	s_cselect_b32 s35, 3, 15
	s_cselect_b32 s37, 2, 4
	s_cmp_lt_u32 s23, 64
	s_cselect_b64 s[28:29], -1, 0
	s_and_b64 s[56:57], s[28:29], exec
	s_cselect_b32 s62, 0, s37
	s_waitcnt vmcnt(2)
	v_mov_b64_e32 v[88:89], v[10:11]
	s_cselect_b32 s23, 0, s35
	s_lshr_b32 s25, s25, s62
	s_waitcnt vmcnt(1)
	v_mov_b64_e32 v[50:51], v[14:15]
	v_mov_b64_e32 v[86:87], v[8:9]
	v_sub_u32_e64 v8, s25, 1 clamp
	v_mov_b64_e32 v[48:49], v[12:13]
	s_ashr_i32 s35, s34, 31
	v_lshlrev_b32_e32 v12, 7, v8
	s_and_b32 s23, s23, s70
	s_lshl_b64 s[56:57], s[34:35], 13
	v_or_b32_e32 v8, v12, v172
	s_or_b32 s56, s56, s23
	v_lshlrev_b32_e32 v64, s62, v8
	v_lshl_add_u64 v[8:9], s[56:57], 0, v[64:65]
	v_lshlrev_b64 v[8:9], 7, v[8:9]
	v_or_b32_e32 v8, v8, v191
	v_lshl_add_u64 v[10:11], s[76:77], 0, v[8:9]
	v_lshl_add_u64 v[8:9], s[78:79], 0, v[8:9]
	global_load_dwordx4 v[16:19], v[10:11], off
	global_load_dwordx4 v[20:23], v[8:9], off
	v_or_b32_e32 v8, v12, v174
	v_lshlrev_b32_e32 v64, s62, v8
	v_lshl_add_u64 v[8:9], s[56:57], 0, v[64:65]
	v_lshlrev_b64 v[8:9], 7, v[8:9]
	v_or_b32_e32 v8, v8, v191
	v_lshl_add_u64 v[10:11], s[76:77], 0, v[8:9]
	v_lshl_add_u64 v[8:9], s[78:79], 0, v[8:9]
	s_lshl_b32 s63, s25, 7
	global_load_dwordx4 v[24:27], v[10:11], off
	global_load_dwordx4 v[28:31], v[8:9], off
	v_or_b32_e32 v8, s63, v172
	v_lshlrev_b32_e32 v64, s62, v8
	v_lshl_add_u64 v[8:9], s[56:57], 0, v[64:65]
	v_lshlrev_b64 v[8:9], 7, v[8:9]
	v_or_b32_e32 v8, v8, v191
	v_lshl_add_u64 v[10:11], s[76:77], 0, v[8:9]
	v_lshl_add_u64 v[8:9], s[78:79], 0, v[8:9]
	global_load_dwordx4 v[32:35], v[10:11], off
	global_load_dwordx4 v[36:39], v[8:9], off
	v_or_b32_e32 v8, s63, v175
	v_lshlrev_b32_e32 v64, s62, v8
	v_lshl_add_u64 v[8:9], s[56:57], 0, v[64:65]
	v_lshlrev_b64 v[8:9], 7, v[8:9]
	v_or_b32_e32 v8, v8, v191
	v_lshl_add_u64 v[10:11], s[76:77], 0, v[8:9]
	v_lshl_add_u64 v[8:9], s[78:79], 0, v[8:9]
	global_load_dwordx4 v[40:43], v[10:11], off
	global_load_dwordx4 v[44:47], v[8:9], off
	s_ashr_i32 s37, s36, 31
	v_add_u32_e32 v8, s63, v181
	s_lshl_b64 s[36:37], s[36:37], 13
	v_ashrrev_i32_e32 v9, 31, v8
	s_or_b32 s36, s36, s23
	v_lshlrev_b64 v[8:9], s62, v[8:9]
	v_lshl_add_u64 v[164:165], s[36:37], 0, v[8:9]
	v_lshlrev_b64 v[162:163], 6, v[164:165]
	s_lshl_b64 s[36:37], s[34:35], 20
	s_add_u32 s36, s64, s36
	v_lshlrev_b32_e32 v8, 1, v162
	s_addc_u32 s37, s65, s37
	v_and_b32_e32 v64, 0xfff80, v8
	v_lshl_add_u64 v[8:9], s[36:37], 0, v[64:65]
	v_mov_b32_e32 v169, v65
	v_lshl_add_u64 v[12:13], v[8:9], 0, v[168:169]
	global_load_dwordx4 v[8:11], v[12:13], off
	s_nop 0
	global_load_dwordx4 v[12:15], v[12:13], off offset:64
	s_mul_i32 s23, s49, 0x12000
	s_add_i32 s23, s23, 0
	v_add3_u32 v56, s23, v182, v215
	v_add3_u32 v64, s23, v183, v215
	ds_read_b128 v[52:55], v56
	ds_read_b128 v[56:59], v56 offset:64
	ds_read_b128 v[60:63], v64
	ds_read_b128 v[66:69], v64 offset:64
	v_add3_u32 v64, s23, v184, v215
	ds_read_b128 v[70:73], v64
	ds_read_b128 v[74:77], v64 offset:64
	v_add3_u32 v64, s23, v185, v215
	ds_read_b128 v[90:93], v64
	ds_read_b128 v[94:97], v64 offset:64
	v_add3_u32 v64, s23, v186, v215
	ds_read_b128 v[98:101], v64
	ds_read_b128 v[102:105], v64 offset:64
	v_add3_u32 v64, s23, v187, v215
	ds_read_b128 v[106:109], v64
	ds_read_b128 v[110:113], v64 offset:64
	v_add3_u32 v64, s23, v188, v215
	ds_read_b128 v[114:117], v64
	ds_read_b128 v[118:121], v64 offset:64
	v_add3_u32 v64, s23, v189, v215
	ds_read_b128 v[122:125], v64
	ds_read_b128 v[126:129], v64 offset:64
	v_add3_u32 v64, s23, v190, v215
	ds_read_b128 v[130:133], v64
	ds_read_b128 v[134:137], v64 offset:64
	s_waitcnt lgkmcnt(14)
	v_mfma_f32_16x16x32_bf16 v[52:55], v[52:55], v[86:89], v[4:7]
	s_cmp_lg_u32 s31, 0
	v_mfma_f32_16x16x32_bf16 v[82:85], v[56:59], v[48:51], v[52:55]
	v_mfma_f32_16x16x32_bf16 v[52:55], v[60:63], v[86:89], 0
	v_mfma_f32_16x16x32_bf16 v[78:81], v[66:69], v[48:51], v[52:55]
	s_waitcnt lgkmcnt(13)
	v_mfma_f32_16x16x32_bf16 v[52:55], v[70:73], v[86:89], 0
	s_waitcnt lgkmcnt(12)
	v_mfma_f32_16x16x32_bf16 v[74:77], v[74:77], v[48:51], v[52:55]
	s_waitcnt lgkmcnt(11)
	v_mfma_f32_16x16x32_bf16 v[52:55], v[90:93], v[86:89], 0
	s_waitcnt lgkmcnt(10)
	v_mfma_f32_16x16x32_bf16 v[70:73], v[94:97], v[48:51], v[52:55]
	s_waitcnt lgkmcnt(9)
	v_mfma_f32_16x16x32_bf16 v[52:55], v[98:101], v[86:89], 0
	s_waitcnt lgkmcnt(8)
	v_mfma_f32_16x16x32_bf16 v[66:69], v[102:105], v[48:51], v[52:55]
	s_waitcnt lgkmcnt(7)
	v_mfma_f32_16x16x32_bf16 v[52:55], v[106:109], v[86:89], 0
	s_waitcnt lgkmcnt(6)
	v_mfma_f32_16x16x32_bf16 v[60:63], v[110:113], v[48:51], v[52:55]
	s_waitcnt lgkmcnt(5)
	v_mfma_f32_16x16x32_bf16 v[52:55], v[114:117], v[86:89], 0
	s_waitcnt lgkmcnt(4)
	v_mfma_f32_16x16x32_bf16 v[56:59], v[118:121], v[48:51], v[52:55]
	s_waitcnt lgkmcnt(3)
	v_mfma_f32_16x16x32_bf16 v[52:55], v[122:125], v[86:89], 0
	s_waitcnt lgkmcnt(1)
	v_mfma_f32_16x16x32_bf16 v[86:89], v[130:133], v[86:89], v[0:3]
	v_mfma_f32_16x16x32_bf16 v[52:55], v[126:129], v[48:51], v[52:55]
	s_waitcnt lgkmcnt(0)
	v_mfma_f32_16x16x32_bf16 v[48:51], v[134:137], v[48:51], v[86:89]
	s_cbranch_scc1 .LBB0_414
	s_nop 3
	v_pk_add_f32 v[86:87], v[84:85], s[84:85] op_sel_hi:[1,0]
	v_pk_add_f32 v[88:89], v[82:83], s[84:85] op_sel_hi:[1,0]
	v_cndmask_b32_e64 v85, v85, v87, s[20:21]
	v_cndmask_b32_e64 v84, v84, v86, s[20:21]
	v_cndmask_b32_e64 v83, v83, v89, s[20:21]
	v_cndmask_b32_e64 v82, v82, v88, s[20:21]
	v_pk_add_f32 v[86:87], v[80:81], s[84:85] op_sel_hi:[1,0]
	v_pk_add_f32 v[88:89], v[78:79], s[84:85] op_sel_hi:[1,0]
	v_cndmask_b32_e64 v81, v81, v87, s[18:19]
	v_cndmask_b32_e64 v80, v80, v86, s[18:19]
	v_cndmask_b32_e64 v79, v79, v89, s[18:19]
	v_cndmask_b32_e64 v78, v78, v88, s[18:19]
	v_pk_add_f32 v[86:87], v[76:77], s[84:85] op_sel_hi:[1,0]
	v_pk_add_f32 v[88:89], v[74:75], s[84:85] op_sel_hi:[1,0]
	v_cndmask_b32_e64 v77, v77, v87, s[16:17]
	v_cndmask_b32_e64 v76, v76, v86, s[16:17]
	v_cndmask_b32_e64 v75, v75, v89, s[16:17]
	v_cndmask_b32_e64 v74, v74, v88, s[16:17]
	v_pk_add_f32 v[86:87], v[72:73], s[84:85] op_sel_hi:[1,0]
	v_pk_add_f32 v[88:89], v[70:71], s[84:85] op_sel_hi:[1,0]
	v_cndmask_b32_e64 v73, v73, v87, s[14:15]
	v_cndmask_b32_e64 v72, v72, v86, s[14:15]
	v_cndmask_b32_e64 v71, v71, v89, s[14:15]
	v_cndmask_b32_e64 v70, v70, v88, s[14:15]
	v_pk_add_f32 v[86:87], v[68:69], s[84:85] op_sel_hi:[1,0]
	v_pk_add_f32 v[88:89], v[66:67], s[84:85] op_sel_hi:[1,0]
	v_cndmask_b32_e64 v69, v69, v87, s[12:13]
	v_cndmask_b32_e64 v68, v68, v86, s[12:13]
	v_cndmask_b32_e64 v67, v67, v89, s[12:13]
	v_cndmask_b32_e64 v66, v66, v88, s[12:13]
	v_pk_add_f32 v[86:87], v[62:63], s[84:85] op_sel_hi:[1,0]
	v_pk_add_f32 v[88:89], v[60:61], s[84:85] op_sel_hi:[1,0]
	v_cndmask_b32_e64 v63, v63, v87, s[10:11]
	v_cndmask_b32_e64 v62, v62, v86, s[10:11]
	v_cndmask_b32_e64 v61, v61, v89, s[10:11]
	v_cndmask_b32_e64 v60, v60, v88, s[10:11]
	v_pk_add_f32 v[86:87], v[58:59], s[84:85] op_sel_hi:[1,0]
	v_pk_add_f32 v[88:89], v[56:57], s[84:85] op_sel_hi:[1,0]
	v_cndmask_b32_e64 v59, v59, v87, s[8:9]
	v_cndmask_b32_e64 v58, v58, v86, s[8:9]
	v_cndmask_b32_e64 v57, v57, v89, s[8:9]
	v_cndmask_b32_e64 v56, v56, v88, s[8:9]
	v_pk_add_f32 v[86:87], v[54:55], s[84:85] op_sel_hi:[1,0]
	v_pk_add_f32 v[88:89], v[52:53], s[84:85] op_sel_hi:[1,0]
	v_cndmask_b32_e64 v55, v55, v87, s[6:7]
	v_cndmask_b32_e64 v54, v54, v86, s[6:7]
	v_cndmask_b32_e64 v53, v53, v89, s[6:7]
	v_cndmask_b32_e64 v52, v52, v88, s[6:7]

.LBB0_418:
	s_add_i32 s23, 0, 0x12000
	v_add3_u32 v20, s23, v182, v215
	v_add3_u32 v28, s23, v183, v215
	v_add3_u32 v36, s23, v184, v215
	ds_read_b128 v[16:19], v20
	ds_read_b128 v[20:23], v20 offset:64
	ds_read_b128 v[24:27], v28
	ds_read_b128 v[28:31], v28 offset:64
	ds_read_b128 v[32:35], v36
	ds_read_b128 v[44:47], v36 offset:64
	v_add3_u32 v36, s23, v185, v215
	ds_read_b128 v[48:51], v36
	ds_read_b128 v[52:55], v36 offset:64
	v_add3_u32 v36, s23, v186, v215
	ds_read_b128 v[56:59], v36
	ds_read_b128 v[60:63], v36 offset:64
	v_add3_u32 v36, s23, v187, v215
	ds_read_b128 v[66:69], v36
	ds_read_b128 v[70:73], v36 offset:64
	v_add3_u32 v36, s23, v188, v215
	ds_read_b128 v[74:77], v36
	ds_read_b128 v[78:81], v36 offset:64
	v_add3_u32 v36, s23, v189, v215
	ds_read_b128 v[82:85], v36
	ds_read_b128 v[86:89], v36 offset:64
	v_add3_u32 v36, s23, v190, v215
	ds_read_b128 v[90:93], v36
	ds_read_b128 v[94:97], v36 offset:64
	s_waitcnt vmcnt(2) lgkmcnt(14)
	v_mfma_f32_16x16x32_bf16 v[4:7], v[16:19], v[8:11], v[4:7]
	s_cmp_lg_u32 s25, 0
	s_waitcnt vmcnt(1)
	v_mfma_f32_16x16x32_bf16 v[40:43], v[20:23], v[12:15], v[4:7]
	v_mfma_f32_16x16x32_bf16 v[4:7], v[24:27], v[8:11], 0
	v_mfma_f32_16x16x32_bf16 v[36:39], v[28:31], v[12:15], v[4:7]
	s_waitcnt lgkmcnt(13)
	v_mfma_f32_16x16x32_bf16 v[4:7], v[32:35], v[8:11], 0
	s_waitcnt lgkmcnt(12)
	v_mfma_f32_16x16x32_bf16 v[32:35], v[44:47], v[12:15], v[4:7]
	s_waitcnt lgkmcnt(11)
	v_mfma_f32_16x16x32_bf16 v[4:7], v[48:51], v[8:11], 0
	s_waitcnt lgkmcnt(10)
	v_mfma_f32_16x16x32_bf16 v[28:31], v[52:55], v[12:15], v[4:7]
	s_waitcnt lgkmcnt(9)
	v_mfma_f32_16x16x32_bf16 v[4:7], v[56:59], v[8:11], 0
	s_waitcnt lgkmcnt(8)
	v_mfma_f32_16x16x32_bf16 v[24:27], v[60:63], v[12:15], v[4:7]
	s_waitcnt lgkmcnt(7)
	v_mfma_f32_16x16x32_bf16 v[4:7], v[66:69], v[8:11], 0
	s_waitcnt lgkmcnt(6)
	v_mfma_f32_16x16x32_bf16 v[20:23], v[70:73], v[12:15], v[4:7]
	s_waitcnt lgkmcnt(5)
	v_mfma_f32_16x16x32_bf16 v[4:7], v[74:77], v[8:11], 0
	s_waitcnt lgkmcnt(4)
	v_mfma_f32_16x16x32_bf16 v[16:19], v[78:81], v[12:15], v[4:7]
	s_waitcnt lgkmcnt(3)
	v_mfma_f32_16x16x32_bf16 v[4:7], v[82:85], v[8:11], 0
	s_waitcnt lgkmcnt(1)
	v_mfma_f32_16x16x32_bf16 v[0:3], v[90:93], v[8:11], v[0:3]
	v_mfma_f32_16x16x32_bf16 v[4:7], v[86:89], v[12:15], v[4:7]
	s_waitcnt lgkmcnt(0)
	v_mfma_f32_16x16x32_bf16 v[0:3], v[94:97], v[12:15], v[0:3]
	s_cbranch_scc1 .LBB0_420
	v_pk_add_f32 v[8:9], v[42:43], s[84:85] op_sel_hi:[1,0]
	v_pk_add_f32 v[10:11], v[40:41], s[84:85] op_sel_hi:[1,0]
	v_cndmask_b32_e64 v43, v43, v9, s[20:21]
	v_cndmask_b32_e64 v42, v42, v8, s[20:21]
	v_cndmask_b32_e64 v41, v41, v11, s[20:21]
	v_cndmask_b32_e64 v40, v40, v10, s[20:21]
	v_pk_add_f32 v[8:9], v[38:39], s[84:85] op_sel_hi:[1,0]
	v_pk_add_f32 v[10:11], v[36:37], s[84:85] op_sel_hi:[1,0]
	v_cndmask_b32_e64 v39, v39, v9, s[18:19]
	v_cndmask_b32_e64 v38, v38, v8, s[18:19]
	v_cndmask_b32_e64 v37, v37, v11, s[18:19]
	v_cndmask_b32_e64 v36, v36, v10, s[18:19]
	v_pk_add_f32 v[8:9], v[34:35], s[84:85] op_sel_hi:[1,0]
	v_pk_add_f32 v[10:11], v[32:33], s[84:85] op_sel_hi:[1,0]
	v_cndmask_b32_e64 v35, v35, v9, s[16:17]
	v_cndmask_b32_e64 v34, v34, v8, s[16:17]
	v_cndmask_b32_e64 v33, v33, v11, s[16:17]
	v_cndmask_b32_e64 v32, v32, v10, s[16:17]
	v_pk_add_f32 v[8:9], v[30:31], s[84:85] op_sel_hi:[1,0]
	v_pk_add_f32 v[10:11], v[28:29], s[84:85] op_sel_hi:[1,0]
	v_cndmask_b32_e64 v31, v31, v9, s[14:15]
	v_cndmask_b32_e64 v30, v30, v8, s[14:15]
	v_cndmask_b32_e64 v29, v29, v11, s[14:15]
	v_cndmask_b32_e64 v28, v28, v10, s[14:15]
	v_pk_add_f32 v[8:9], v[26:27], s[84:85] op_sel_hi:[1,0]
	v_pk_add_f32 v[10:11], v[24:25], s[84:85] op_sel_hi:[1,0]
	v_cndmask_b32_e64 v27, v27, v9, s[12:13]
	v_cndmask_b32_e64 v26, v26, v8, s[12:13]
	v_cndmask_b32_e64 v25, v25, v11, s[12:13]
	v_cndmask_b32_e64 v24, v24, v10, s[12:13]
	v_pk_add_f32 v[8:9], v[22:23], s[84:85] op_sel_hi:[1,0]
	v_pk_add_f32 v[10:11], v[20:21], s[84:85] op_sel_hi:[1,0]
	v_cndmask_b32_e64 v23, v23, v9, s[10:11]
	v_cndmask_b32_e64 v22, v22, v8, s[10:11]
	v_cndmask_b32_e64 v21, v21, v11, s[10:11]
	v_cndmask_b32_e64 v20, v20, v10, s[10:11]
	v_pk_add_f32 v[8:9], v[18:19], s[84:85] op_sel_hi:[1,0]
	v_pk_add_f32 v[10:11], v[16:17], s[84:85] op_sel_hi:[1,0]
	v_cndmask_b32_e64 v19, v19, v9, s[8:9]
	v_cndmask_b32_e64 v18, v18, v8, s[8:9]
	v_cndmask_b32_e64 v17, v17, v11, s[8:9]
	v_cndmask_b32_e64 v16, v16, v10, s[8:9]
	v_pk_add_f32 v[8:9], v[6:7], s[84:85] op_sel_hi:[1,0]
	v_pk_add_f32 v[10:11], v[4:5], s[84:85] op_sel_hi:[1,0]
	v_cndmask_b32_e64 v7, v7, v9, s[6:7]
	v_cndmask_b32_e64 v6, v6, v8, s[6:7]
	v_cndmask_b32_e64 v5, v5, v11, s[6:7]
	v_cndmask_b32_e64 v4, v4, v10, s[6:7]

.LBB0_824:
	v_readlane_b32 s4, v255, 0
	s_add_i32 s50, s50, 1
	s_nop 0
	v_mov_b32_e32 v0, s4
	ds_read_b32 v0, v0
	s_mul_i32 s4, s50, s44
	s_add_i32 s4, s4, s70
	s_waitcnt lgkmcnt(0)
	v_readfirstlane_b32 s5, v0
	s_lshl_b32 s5, s5, 2
	s_cmp_lt_i32 s4, s5
	s_cselect_b64 s[22:23], -1, 0
	s_cmp_ge_i32 s4, s5
	s_cbranch_scc1 .LBB0_826
	s_ashr_i32 s10, s4, 2
	s_and_b32 s4, s4, 3
	v_mbcnt_lo_u32_b32 v0, -1, 0
	v_mbcnt_hi_u32_b32 v0, -1, v0
	v_and_b32_e32 v0, 31, v0
	v_lshlrev_b32_e32 v0, 2, v0
	v_add_u32_e32 v0, 0x25000, v0
	ds_read_b32 v1, v0
	s_waitcnt lgkmcnt(0)
	v_cmp_ge_i32_e32 vcc, s10, v1
	s_nop 3
	s_and_b32 s5, vcc_lo, 0xfffffffe
	s_bcnt1_i32_b32 s5, s5
	s_lshl_b32 s5, s5, 2
	s_or_b32 s12, s5, s4

.LBB0_897:
	v_readlane_b32 s4, v255, 0
	s_add_i32 s66, s66, 1
	s_nop 0
	v_mov_b32_e32 v0, s4
	ds_read_b32 v0, v0
	s_mul_i32 s4, s66, s44
	s_add_i32 s4, s4, s59
	s_waitcnt lgkmcnt(0)
	v_readfirstlane_b32 s5, v0
	s_lshl_b32 s5, s5, 2
	s_cmp_lt_i32 s4, s5
	s_cselect_b64 s[16:17], -1, 0
	s_cmp_ge_i32 s4, s5
	s_cbranch_scc1 .LBB0_899
	s_ashr_i32 s70, s4, 2
	s_and_b32 s4, s4, 3
	v_mbcnt_lo_u32_b32 v0, -1, 0
	v_mbcnt_hi_u32_b32 v0, -1, v0
	v_and_b32_e32 v0, 31, v0
	v_lshlrev_b32_e32 v0, 2, v0
	v_add_u32_e32 v0, 0x25000, v0
	ds_read_b32 v1, v0
	s_waitcnt lgkmcnt(0)
	v_cmp_ge_i32_e32 vcc, s70, v1
	s_nop 3
	s_and_b32 s5, vcc_lo, 0xfffffffe
	s_bcnt1_i32_b32 s5, s5
	s_lshl_b32 s5, s5, 2
	s_or_b32 s86, s5, s4
